# v59 + memory-token rmsnorm rows: all x and gain loads of a row in flight together; block-compression K loop pipelined; MoeOrder row-tile lookup by one lane-indexed LDS read + popcount instead of 15 se
# speedup vs baseline: 1.0198x; 1.0034x over previous
.LBB0_3598:
	global_load_dwordx4 v[10:13], v[50:51], off offset:-4080
	global_load_dwordx4 v[18:21], v[50:51], off offset:-4096
	global_load_dwordx4 v[2:5], v[50:51], off offset:-2032
	global_load_dwordx4 v[22:25], v[50:51], off offset:-2048
	global_load_dwordx4 v[6:9], v[50:51], off offset:16
	global_load_dwordx4 v[26:29], v[50:51], off
	global_load_dwordx4 v[14:17], v[50:51], off offset:2064
	global_load_dwordx4 v[30:33], v[50:51], off offset:2048
	global_load_dwordx4 v[156:159], v[42:43], off offset:16
	global_load_dwordx4 v[160:163], v[42:43], off
	global_load_dwordx4 v[164:167], v[42:43], off offset:2064
	global_load_dwordx4 v[168:171], v[42:43], off offset:2048
	global_load_dwordx4 v[172:175], v[44:45], off offset:16
	global_load_dwordx4 v[176:179], v[44:45], off
	global_load_dwordx4 v[180:183], v[46:47], off offset:16
	global_load_dwordx4 v[184:187], v[46:47], off
	s_add_i32 s4, s4, s12
	s_cmpk_gt_i32 s4, 0x7ff
	s_waitcnt vmcnt(14)
	v_mul_f32_e32 v0, v19, v19
	v_mul_f32_e32 v188, v21, v21
	v_fmac_f32_e32 v0, v18, v18
	v_fmac_f32_e32 v188, v20, v20
	v_add_f32_e32 v0, v0, v188
	v_mul_f32_e32 v188, v11, v11
	v_fmac_f32_e32 v188, v10, v10
	v_add_f32_e32 v0, v0, v188
	v_mul_f32_e32 v188, v13, v13
	v_fmac_f32_e32 v188, v12, v12
	v_add_f32_e32 v0, v188, v0
	s_waitcnt vmcnt(12)
	v_mul_f32_e32 v188, v23, v23
	v_fmac_f32_e32 v188, v22, v22
	v_add_f32_e32 v0, v188, v0
	v_mul_f32_e32 v188, v25, v25
	v_fmac_f32_e32 v188, v24, v24
	v_add_f32_e32 v0, v188, v0
	v_mul_f32_e32 v188, v3, v3
	v_fmac_f32_e32 v188, v2, v2
	v_add_f32_e32 v0, v188, v0
	v_mul_f32_e32 v188, v5, v5
	v_fmac_f32_e32 v188, v4, v4
	v_add_f32_e32 v0, v188, v0
	s_waitcnt vmcnt(10)
	v_mul_f32_e32 v188, v27, v27
	v_fmac_f32_e32 v188, v26, v26
	v_add_f32_e32 v0, v188, v0
	v_mul_f32_e32 v188, v29, v29
	v_fmac_f32_e32 v188, v28, v28
	v_add_f32_e32 v0, v188, v0
	v_mul_f32_e32 v188, v7, v7
	v_fmac_f32_e32 v188, v6, v6
	v_add_f32_e32 v0, v188, v0
	v_mul_f32_e32 v188, v9, v9
	v_fmac_f32_e32 v188, v8, v8
	v_add_f32_e32 v0, v188, v0
	v_lshl_add_u64 v[50:51], v[50:51], 0, s[86:87]
	s_waitcnt vmcnt(8)
	v_pk_mul_f32 v[34:35], v[32:33], v[32:33]
	v_pk_mul_f32 v[36:37], v[30:31], v[30:31]
	v_mov_b32_e32 v38, v34
	v_mov_b32_e32 v39, v36
	v_mov_b32_e32 v36, v35
	v_pk_add_f32 v[34:35], v[38:39], v[36:37]
	v_pk_mul_f32 v[36:37], v[14:15], v[14:15]
	v_add_f32_e32 v0, v35, v0
	v_add_f32_e32 v0, v34, v0
	v_pk_mul_f32 v[34:35], v[16:17], v[16:17]
	v_mov_b32_e32 v39, v36
	v_mov_b32_e32 v38, v34
	v_mov_b32_e32 v36, v35
	v_pk_add_f32 v[34:35], v[38:39], v[36:37]
	s_nop 0
	v_add_f32_e32 v0, v35, v0
	v_add_f32_e32 v0, v34, v0
	ds_bpermute_b32 v34, v52, v0
	s_waitcnt lgkmcnt(0)
	v_add_f32_e32 v0, v0, v34
	ds_bpermute_b32 v34, v53, v0
	s_waitcnt lgkmcnt(0)
	v_add_f32_e32 v0, v0, v34
	ds_bpermute_b32 v34, v54, v0
	s_waitcnt lgkmcnt(0)
	v_add_f32_e32 v0, v0, v34
	ds_bpermute_b32 v34, v56, v0
	s_waitcnt lgkmcnt(0)
	v_add_f32_e32 v0, v0, v34
	ds_bpermute_b32 v34, v60, v0
	s_waitcnt lgkmcnt(0)
	v_add_f32_e32 v0, v0, v34
	ds_bpermute_b32 v34, v61, v0
	s_waitcnt lgkmcnt(0)
	v_add_f32_e32 v0, v0, v34
	v_fmamk_f32 v0, v0, 0x3a000000, v220
	v_cmp_gt_f32_e32 vcc, s65, v0
	v_mul_f32_e32 v34, 0x4b800000, v0
	s_nop 0
	v_cndmask_b32_e32 v0, v0, v34, vcc
	v_rsq_f32_e32 v0, v0
	s_nop 0
	v_mul_f32_e32 v34, 0x45800000, v0
	v_cndmask_b32_e32 v0, v0, v34, vcc
	v_pk_mul_f32 v[10:11], v[10:11], v[0:1] op_sel_hi:[1,0]
	v_pk_mul_f32 v[18:19], v[18:19], v[0:1] op_sel_hi:[1,0]
	v_pk_mul_f32 v[2:3], v[2:3], v[0:1] op_sel_hi:[1,0]
	v_pk_mul_f32 v[22:23], v[22:23], v[0:1] op_sel_hi:[1,0]
	v_pk_mul_f32 v[6:7], v[6:7], v[0:1] op_sel_hi:[1,0]
	s_waitcnt vmcnt(7)
	v_pk_mul_f32 v[34:35], v[156:157], v[10:11]
	v_pk_mul_f32 v[10:11], v[20:21], v[0:1] op_sel_hi:[1,0]
	s_waitcnt vmcnt(6)
	v_pk_mul_f32 v[18:19], v[160:161], v[18:19]
	v_pk_mul_f32 v[20:21], v[162:163], v[10:11]
	v_pk_mul_f32 v[10:11], v[12:13], v[0:1] op_sel_hi:[1,0]
	v_cvt_pk_bf16_f32 v12, v34, v35
	v_pk_mul_f32 v[36:37], v[158:159], v[10:11]
	v_cvt_pk_bf16_f32 v10, v18, v19
	v_cvt_pk_bf16_f32 v11, v20, v21
	v_cvt_pk_bf16_f32 v13, v36, v37
	global_store_dwordx4 v[48:49], v[10:13], off
	s_nop 1
	s_waitcnt vmcnt(5)
	v_pk_mul_f32 v[10:11], v[164:165], v[2:3]
	v_pk_mul_f32 v[2:3], v[24:25], v[0:1] op_sel_hi:[1,0]
	s_waitcnt vmcnt(4)
	v_pk_mul_f32 v[18:19], v[168:169], v[22:23]
	v_pk_mul_f32 v[20:21], v[170:171], v[2:3]
	v_pk_mul_f32 v[2:3], v[4:5], v[0:1] op_sel_hi:[1,0]
	v_cvt_pk_bf16_f32 v4, v10, v11
	v_pk_mul_f32 v[12:13], v[166:167], v[2:3]
	v_cvt_pk_bf16_f32 v2, v18, v19
	v_cvt_pk_bf16_f32 v3, v20, v21
	v_cvt_pk_bf16_f32 v5, v12, v13
	global_store_dwordx4 v[48:49], v[2:5], off offset:1024
	s_nop 0
	v_pk_mul_f32 v[18:19], v[26:27], v[0:1] op_sel_hi:[1,0]
	s_waitcnt vmcnt(3)
	v_pk_mul_f32 v[6:7], v[172:173], v[6:7]
	v_pk_mul_f32 v[2:3], v[28:29], v[0:1] op_sel_hi:[1,0]
	s_waitcnt vmcnt(2)
	v_pk_mul_f32 v[10:11], v[176:177], v[18:19]
	v_pk_mul_f32 v[12:13], v[178:179], v[2:3]
	v_pk_mul_f32 v[2:3], v[8:9], v[0:1] op_sel_hi:[1,0]
	s_nop 0
	v_pk_mul_f32 v[8:9], v[174:175], v[2:3]
	v_cvt_pk_bf16_f32 v2, v10, v11
	v_cvt_pk_bf16_f32 v3, v12, v13
	v_cvt_pk_bf16_f32 v4, v6, v7
	v_cvt_pk_bf16_f32 v5, v8, v9
	global_store_dwordx4 v[48:49], v[2:5], off offset:2048
	v_pk_mul_f32 v[10:11], v[30:31], v[0:1] op_sel_hi:[1,0]
	s_waitcnt vmcnt(0)
	v_pk_mul_f32 v[6:7], v[184:185], v[10:11]
	v_pk_mul_f32 v[10:11], v[14:15], v[0:1] op_sel_hi:[1,0]
	s_nop 0
	v_pk_mul_f32 v[10:11], v[180:181], v[10:11]
	v_pk_mul_f32 v[2:3], v[32:33], v[0:1] op_sel_hi:[1,0]
	s_nop 0
	v_pk_mul_f32 v[8:9], v[186:187], v[2:3]
	v_pk_mul_f32 v[2:3], v[16:17], v[0:1] op_sel_hi:[1,0]
	s_nop 0
	v_pk_mul_f32 v[12:13], v[182:183], v[2:3]
	v_cvt_pk_bf16_f32 v2, v6, v7
	v_cvt_pk_bf16_f32 v3, v8, v9
	v_cvt_pk_bf16_f32 v4, v10, v11
	v_cvt_pk_bf16_f32 v5, v12, v13
	global_store_dwordx4 v[48:49], v[2:5], off offset:3072
	v_lshl_add_u64 v[48:49], v[48:49], 0, s[74:75]
	s_cbranch_scc0 .LBB0_3598

.LBB0_5215:
	s_add_i32 s59, s59, 1
	s_mul_i32 s0, s59, s95
	s_add_i32 s0, s0, s42
	s_cmp_ge_i32 s0, s41
	s_mov_b64 s[26:27], 0
	s_cbranch_scc1 .LBB0_5218
	s_add_i32 s0, s0, s58
	s_cmp_ge_i32 s0, s43
	s_cbranch_scc1 .LBB0_5218
	s_add_i32 s24, 0, 0x20200
	v_lshl_add_u32 v2, v218, 2, s24
	ds_read_b32 v3, v2
	s_ashr_i32 s60, s0, 3
	s_mov_b64 s[26:27], -1
	s_and_b32 s0, s0, 7
	s_waitcnt lgkmcnt(0)
	v_cmp_ge_i32_e32 vcc, s60, v3
	s_nop 1
	s_and_b32 s24, vcc_lo, 0xfffe
	s_bcnt1_i32_b32 s62, s24
	s_lshl_b32 s24, s62, 3
	s_or_b32 s24, s24, s0
	s_nop 1
	v_readlane_b32 s0, v3, s62
	s_sub_i32 s63, s60, s0

.LBB0_6151:
	s_add_i32 s56, s56, 1
	s_mul_i32 s0, s56, s95
	s_add_i32 s0, s0, s38
	s_cmp_ge_i32 s0, s37
	s_mov_b64 s[26:27], 0
	s_cbranch_scc1 .LBB0_6154
	s_add_i32 s0, s0, s40
	s_cmp_ge_i32 s0, s39
	s_cbranch_scc1 .LBB0_6154
	v_lshl_add_u32 v2, v218, 2, s43
	ds_read_b32 v3, v2
	s_ashr_i32 s57, s0, 3
	s_mov_b64 s[26:27], -1
	s_and_b32 s0, s0, 7
	s_waitcnt lgkmcnt(0)
	v_cmp_ge_i32_e32 vcc, s57, v3
	s_nop 1
	s_and_b32 s22, vcc_lo, 0xfffe
	s_bcnt1_i32_b32 s21, s22
	s_lshl_b32 s22, s21, 3
	s_or_b32 s22, s22, s0
